# select bounds via v_cvt_f16_i16 + op_sel_hi broadcast (2 fewer VALU per select setup), on top of balanced chunk pairing
# speedup vs baseline: 1.0145x; 1.0055x over previous
.Lcs_done:
	global_load_dword v241, v4, s[54:55]
	s_add_i32 s18, s13, 32
	s_add_i32 s19, s13, 16
	s_mov_b64 s[6:7], 0
	v_mfma_f32_32x32x16_f16 v[82:97], v[194:197], v[178:181], 0
	v_mfma_f32_32x32x16_f16 v[98:113], v[194:197], v[182:185], 0
	v_add_u32_e32 v14, s13, v243
	v_sub_u32_e32 v3, v230, v14
	v_add_u32_e32 v4, v3, v234
	v_add_u32_e32 v5, -1, v3
	v_med3_i32 v4, v4, -1, 32
	v_med3_i32 v5, v5, -1, 32
	v_cvt_f16_i16_e32 v14, v4
	v_cvt_f16_i16_e32 v15, v5
	v_pk_add_f16 v3, v14, v15 op_sel_hi:[0,0]
	v_pk_mul_f16 v4, v14, v15 op_sel_hi:[0,0]
	v_pk_add_f16 v5, v3, s73 neg_lo:[0,1] neg_hi:[0,1]
	v_pk_add_f16 v16, v3, s74 neg_lo:[0,1] neg_hi:[0,1]
	v_pk_fma_f16 v6, v5, s73, v4 neg_lo:[0,0,1] neg_hi:[0,0,1] clamp
	v_pk_add_f16 v5, v3, s75 neg_lo:[0,1] neg_hi:[0,1]
	v_pk_fma_f16 v7, v16, s74, v4 neg_lo:[0,0,1] neg_hi:[0,0,1] clamp
	v_pk_add_f16 v16, v3, s76 neg_lo:[0,1] neg_hi:[0,1]
	v_pk_fma_f16 v8, v5, s75, v4 neg_lo:[0,0,1] neg_hi:[0,0,1] clamp
	v_pk_add_f16 v5, v3, s77 neg_lo:[0,1] neg_hi:[0,1]
	v_pk_fma_f16 v9, v16, s76, v4 neg_lo:[0,0,1] neg_hi:[0,0,1] clamp
	v_pk_add_f16 v16, v3, s78 neg_lo:[0,1] neg_hi:[0,1]
	v_pk_fma_f16 v10, v5, s77, v4 neg_lo:[0,0,1] neg_hi:[0,0,1] clamp
	v_pk_add_f16 v5, v3, s79 neg_lo:[0,1] neg_hi:[0,1]
	v_pk_fma_f16 v11, v16, s78, v4 neg_lo:[0,0,1] neg_hi:[0,0,1] clamp
	v_pk_add_f16 v16, v3, s80 neg_lo:[0,1] neg_hi:[0,1]
	v_pk_fma_f16 v12, v5, s79, v4 neg_lo:[0,0,1] neg_hi:[0,0,1] clamp
	v_pk_fma_f16 v13, v16, s80, v4 neg_lo:[0,0,1] neg_hi:[0,0,1] clamp
	v_exp_f32_e32 v82, v82
	v_exp_f32_e32 v83, v83
	v_exp_f32_e32 v84, v84
	v_exp_f32_e32 v85, v85
	v_exp_f32_e32 v86, v86
	v_exp_f32_e32 v87, v87
	v_exp_f32_e32 v88, v88
	v_exp_f32_e32 v89, v89
	v_exp_f32_e32 v90, v90
	v_exp_f32_e32 v91, v91
	v_exp_f32_e32 v92, v92
	v_exp_f32_e32 v93, v93
	v_exp_f32_e32 v94, v94
	v_exp_f32_e32 v95, v95
	v_exp_f32_e32 v96, v96
	v_exp_f32_e32 v97, v97
	v_pk_add_f32 v[82:83], v[82:83], s[82:83]
	v_pk_add_f32 v[84:85], v[84:85], s[82:83]
	v_pk_add_f32 v[86:87], v[86:87], s[82:83]
	v_pk_add_f32 v[88:89], v[88:89], s[82:83]
	v_pk_add_f32 v[90:91], v[90:91], s[82:83]
	v_pk_add_f32 v[92:93], v[92:93], s[82:83]
	v_pk_add_f32 v[94:95], v[94:95], s[82:83]
	v_pk_add_f32 v[96:97], v[96:97], s[82:83]
	v_rcp_f32_e32 v82, v82
	v_rcp_f32_e32 v83, v83
	v_rcp_f32_e32 v84, v84
	v_rcp_f32_e32 v85, v85
	v_rcp_f32_e32 v86, v86
	v_rcp_f32_e32 v87, v87
	v_rcp_f32_e32 v88, v88
	v_rcp_f32_e32 v89, v89
	v_rcp_f32_e32 v90, v90
	v_rcp_f32_e32 v91, v91
	v_rcp_f32_e32 v92, v92
	v_rcp_f32_e32 v93, v93
	v_rcp_f32_e32 v94, v94
	v_rcp_f32_e32 v95, v95
	v_rcp_f32_e32 v96, v96
	v_rcp_f32_e32 v97, v97
	v_cvt_pk_f16_f32 v198, v82, v83
	v_cvt_pk_f16_f32 v199, v84, v85
	v_cvt_pk_f16_f32 v200, v86, v87
	v_cvt_pk_f16_f32 v201, v88, v89
	v_cvt_pk_f16_f32 v202, v90, v91
	v_cvt_pk_f16_f32 v203, v92, v93
	v_cvt_pk_f16_f32 v204, v94, v95
	v_cvt_pk_f16_f32 v205, v96, v97
	v_mfma_f32_32x32x16_f16 v[82:97], v[194:197], v[186:189], 0
	v_exp_f32_e32 v98, v98
	v_exp_f32_e32 v99, v99
	v_exp_f32_e32 v100, v100
	v_exp_f32_e32 v101, v101
	v_exp_f32_e32 v102, v102
	v_exp_f32_e32 v103, v103
	v_mfma_f32_32x32x16_f16 v[66:81], v[198:201], v[6:9], v[66:81]
	v_exp_f32_e32 v104, v104
	v_exp_f32_e32 v105, v105
	v_exp_f32_e32 v106, v106
	v_exp_f32_e32 v107, v107
	v_exp_f32_e32 v108, v108
	v_exp_f32_e32 v109, v109
	v_mfma_f32_32x32x16_f16 v[66:81], v[202:205], v[10:13], v[66:81]
	v_exp_f32_e32 v110, v110
	v_exp_f32_e32 v111, v111
	v_exp_f32_e32 v112, v112
	v_exp_f32_e32 v113, v113
	v_pk_add_f32 v[98:99], v[98:99], s[82:83]
	v_pk_add_f32 v[100:101], v[100:101], s[82:83]
	v_pk_add_f32 v[102:103], v[102:103], s[82:83]
	v_pk_add_f32 v[104:105], v[104:105], s[82:83]
	v_pk_add_f32 v[106:107], v[106:107], s[82:83]
	v_pk_add_f32 v[108:109], v[108:109], s[82:83]
	v_pk_add_f32 v[110:111], v[110:111], s[82:83]
	v_pk_add_f32 v[112:113], v[112:113], s[82:83]
	v_rcp_f32_e32 v98, v98
	v_rcp_f32_e32 v99, v99
	v_rcp_f32_e32 v100, v100
	v_rcp_f32_e32 v101, v101
	v_rcp_f32_e32 v102, v102
	v_rcp_f32_e32 v103, v103
	v_rcp_f32_e32 v104, v104
	v_rcp_f32_e32 v105, v105
	v_rcp_f32_e32 v106, v106
	v_rcp_f32_e32 v107, v107
	v_rcp_f32_e32 v108, v108
	v_rcp_f32_e32 v109, v109
	v_rcp_f32_e32 v110, v110
	v_rcp_f32_e32 v111, v111
	v_rcp_f32_e32 v112, v112
	v_rcp_f32_e32 v113, v113
	v_cvt_pk_f16_f32 v206, v98, v99
	v_cvt_pk_f16_f32 v207, v100, v101
	v_cvt_pk_f16_f32 v208, v102, v103
	v_cvt_pk_f16_f32 v209, v104, v105
	v_cvt_pk_f16_f32 v210, v106, v107
	v_cvt_pk_f16_f32 v211, v108, v109
	v_cvt_pk_f16_f32 v212, v110, v111
	v_cvt_pk_f16_f32 v213, v112, v113
	v_mfma_f32_32x32x16_f16 v[98:113], v[194:197], v[190:193], 0
	v_exp_f32_e32 v82, v82
	v_exp_f32_e32 v83, v83
	v_exp_f32_e32 v84, v84
	v_exp_f32_e32 v85, v85
	v_exp_f32_e32 v86, v86
	v_exp_f32_e32 v87, v87
	v_mfma_f32_32x32x16_f16 v[50:65], v[206:209], v[6:9], v[50:65]
	v_exp_f32_e32 v88, v88
	v_exp_f32_e32 v89, v89
	v_exp_f32_e32 v90, v90
	v_exp_f32_e32 v91, v91
	v_exp_f32_e32 v92, v92
	v_exp_f32_e32 v93, v93
	v_mfma_f32_32x32x16_f16 v[50:65], v[210:213], v[10:13], v[50:65]
	v_exp_f32_e32 v94, v94
	v_exp_f32_e32 v95, v95
	v_exp_f32_e32 v96, v96
	v_exp_f32_e32 v97, v97
	v_pk_add_f32 v[82:83], v[82:83], s[82:83]
	v_pk_add_f32 v[84:85], v[84:85], s[82:83]
	v_pk_add_f32 v[86:87], v[86:87], s[82:83]
	v_pk_add_f32 v[88:89], v[88:89], s[82:83]
	v_pk_add_f32 v[90:91], v[90:91], s[82:83]
	v_pk_add_f32 v[92:93], v[92:93], s[82:83]
	v_pk_add_f32 v[94:95], v[94:95], s[82:83]
	v_pk_add_f32 v[96:97], v[96:97], s[82:83]
	v_rcp_f32_e32 v82, v82
	v_rcp_f32_e32 v83, v83
	v_rcp_f32_e32 v84, v84
	v_rcp_f32_e32 v85, v85
	v_rcp_f32_e32 v86, v86
	v_rcp_f32_e32 v87, v87
	v_rcp_f32_e32 v88, v88
	v_rcp_f32_e32 v89, v89
	v_rcp_f32_e32 v90, v90
	v_rcp_f32_e32 v91, v91
	v_rcp_f32_e32 v92, v92
	v_rcp_f32_e32 v93, v93
	v_rcp_f32_e32 v94, v94
	v_rcp_f32_e32 v95, v95
	v_rcp_f32_e32 v96, v96
	v_rcp_f32_e32 v97, v97
	v_cvt_pk_f16_f32 v214, v82, v83
	v_cvt_pk_f16_f32 v215, v84, v85
	v_cvt_pk_f16_f32 v216, v86, v87
	v_cvt_pk_f16_f32 v217, v88, v89
	v_cvt_pk_f16_f32 v218, v90, v91
	v_cvt_pk_f16_f32 v219, v92, v93
	v_cvt_pk_f16_f32 v220, v94, v95
	v_cvt_pk_f16_f32 v221, v96, v97
	v_exp_f32_e32 v98, v98
	v_exp_f32_e32 v99, v99
	v_exp_f32_e32 v100, v100
	v_exp_f32_e32 v101, v101
	v_exp_f32_e32 v102, v102
	v_exp_f32_e32 v103, v103
	v_mfma_f32_32x32x16_f16 v[34:49], v[214:217], v[6:9], v[34:49]
	v_exp_f32_e32 v104, v104
	v_exp_f32_e32 v105, v105
	v_exp_f32_e32 v106, v106
	v_exp_f32_e32 v107, v107
	v_exp_f32_e32 v108, v108
	v_exp_f32_e32 v109, v109
	v_mfma_f32_32x32x16_f16 v[34:49], v[218:221], v[10:13], v[34:49]
	v_exp_f32_e32 v110, v110
	v_exp_f32_e32 v111, v111
	v_exp_f32_e32 v112, v112
	v_exp_f32_e32 v113, v113
	v_pk_add_f32 v[98:99], v[98:99], s[82:83]
	v_pk_add_f32 v[100:101], v[100:101], s[82:83]
	v_pk_add_f32 v[102:103], v[102:103], s[82:83]
	v_pk_add_f32 v[104:105], v[104:105], s[82:83]
	v_pk_add_f32 v[106:107], v[106:107], s[82:83]
	v_pk_add_f32 v[108:109], v[108:109], s[82:83]
	v_pk_add_f32 v[110:111], v[110:111], s[82:83]
	v_pk_add_f32 v[112:113], v[112:113], s[82:83]
	v_rcp_f32_e32 v98, v98
	v_rcp_f32_e32 v99, v99
	v_rcp_f32_e32 v100, v100
	v_rcp_f32_e32 v101, v101
	v_rcp_f32_e32 v102, v102
	v_rcp_f32_e32 v103, v103
	v_rcp_f32_e32 v104, v104
	v_rcp_f32_e32 v105, v105
	v_rcp_f32_e32 v106, v106
	v_rcp_f32_e32 v107, v107
	v_rcp_f32_e32 v108, v108
	v_rcp_f32_e32 v109, v109
	v_rcp_f32_e32 v110, v110
	v_rcp_f32_e32 v111, v111
	v_rcp_f32_e32 v112, v112
	v_rcp_f32_e32 v113, v113
	v_cvt_pk_f16_f32 v222, v98, v99
	v_cvt_pk_f16_f32 v223, v100, v101
	v_cvt_pk_f16_f32 v224, v102, v103
	v_cvt_pk_f16_f32 v225, v104, v105
	v_cvt_pk_f16_f32 v226, v106, v107
	v_cvt_pk_f16_f32 v227, v108, v109
	v_cvt_pk_f16_f32 v228, v110, v111
	v_cvt_pk_f16_f32 v229, v112, v113
	v_mfma_f32_32x32x16_f16 v[18:33], v[222:225], v[6:9], v[18:33]
	v_add_u32_e32 v194, s13, v243
	v_mfma_f32_32x32x16_f16 v[18:33], v[226:229], v[10:13], v[18:33]
	s_cmp_ge_i32 s18, s71
	s_cbranch_scc1 .Lflush

.LBB1_149:
	v_sub_u32_e32 v3, v230, v194
	s_waitcnt lgkmcnt(0)
	v_add_u32_e32 v4, v3, v234
	v_add_u32_e32 v5, -1, v3
	v_med3_i32 v4, v4, -1, 32
	v_med3_i32 v5, v5, -1, 32
	v_cvt_f16_i16_e32 v14, v4
	v_cvt_f16_i16_e32 v15, v5
	v_pk_add_f16 v3, v14, v15 op_sel_hi:[0,0]
	v_pk_mul_f16 v4, v14, v15 op_sel_hi:[0,0]
	v_pk_add_f16 v5, v3, s73 neg_lo:[0,1] neg_hi:[0,1]
	v_pk_add_f16 v16, v3, s74 neg_lo:[0,1] neg_hi:[0,1]
	v_pk_fma_f16 v6, v5, s73, v4 neg_lo:[0,0,1] neg_hi:[0,0,1] clamp
	v_pk_add_f16 v5, v3, s75 neg_lo:[0,1] neg_hi:[0,1]
	v_pk_fma_f16 v7, v16, s74, v4 neg_lo:[0,0,1] neg_hi:[0,0,1] clamp
	v_pk_add_f16 v16, v3, s76 neg_lo:[0,1] neg_hi:[0,1]
	v_pk_fma_f16 v8, v5, s75, v4 neg_lo:[0,0,1] neg_hi:[0,0,1] clamp
	v_pk_fma_f16 v9, v16, s76, v4 neg_lo:[0,0,1] neg_hi:[0,0,1] clamp
	s_nop 1
	v_mfma_f32_32x32x16_f16 v[66:81], v[198:201], v[6:9], 0
	v_mfma_f32_32x32x16_f16 v[50:65], v[206:209], v[6:9], 0
	v_mfma_f32_32x32x16_f16 v[34:49], v[214:217], v[6:9], 0
	v_mfma_f32_32x32x16_f16 v[18:33], v[222:225], v[6:9], 0
